# baseline (speedup 1.0000x reference)
.Lgru_tile:
	s_mov_b32 s92, 0
	s_cmp_eq_u32 s47, 2
	s_cselect_b32 s93, 17, 2
	s_cmp_eq_u32 s47, 1
	s_cselect_b32 s67, 10, 21
	s_cmp_lg_u32 s46, 0
	s_cbranch_scc1 .Lgru_tile_alt
	s_load_dwordx8 s[8:15], s[0:1], 0x0
	s_load_dwordx2 s[2:3], s[0:1], 0x20
	v_lshlrev_b32_e32 v52, 4, v0
	v_mov_b32_e32 v53, 0
	s_movk_i32 s6, 0x100
	s_waitcnt lgkmcnt(0)
	v_lshl_add_u64 v[30:31], s[14:15], 0, v[52:53]
	v_add_co_u32_e32 v14, vcc, 0x2000, v30
	v_bfe_u32 v55, v0, 6, 2
	s_nop 0
	v_addc_co_u32_e32 v15, vcc, 0, v31, vcc
	v_add_co_u32_e32 v22, vcc, 0x6000, v30
	v_mov_b32_e32 v46, s3
	s_nop 0
	v_addc_co_u32_e32 v23, vcc, 0, v31, vcc
	v_add_co_u32_e32 v32, vcc, 0xa000, v30
	v_mov_b32_e32 v47, s13
	s_nop 0
	v_addc_co_u32_e32 v33, vcc, 0, v31, vcc
	v_add_co_u32_e32 v38, vcc, 0xe000, v30
	v_mov_b32_e32 v48, s12
	s_nop 0
	v_addc_co_u32_e32 v39, vcc, 0, v31, vcc
	v_cmp_gt_u32_e32 vcc, s6, v0
	v_mul_u32_u24_e32 v54, 0x540, v55
	v_mov_b32_e32 v49, v53
	v_cndmask_b32_e32 v47, v46, v47, vcc
	v_mov_b32_e32 v46, s2
	v_cndmask_b32_e32 v46, v46, v48, vcc
	v_lshlrev_b32_e32 v48, 4, v54
	v_lshl_add_u64 v[46:47], v[46:47], 0, v[48:49]
	v_lshlrev_b32_e32 v50, 4, v1
	v_mov_b32_e32 v51, v53
	s_movk_i32 s5, 0x1000
	v_lshl_add_u64 v[46:47], v[46:47], 0, v[50:51]
	v_add_co_u32_e32 v48, vcc, s5, v46
	s_movk_i32 s4, 0x2000
	s_nop 0
	v_addc_co_u32_e32 v49, vcc, 0, v47, vcc
	v_or_b32_e32 v56, 0x400, v0
	v_add_co_u32_e32 v60, vcc, s4, v46
	v_lshlrev_b32_e32 v16, 4, v56
	v_or_b32_e32 v24, 0x8000, v52
	v_or_b32_e32 v34, 0xc000, v52
	v_or_b32_e32 v30, 0x1000, v0
	v_addc_co_u32_e32 v61, vcc, 0, v47, vcc
	s_movk_i32 s2, 0x3000
	global_load_dwordx4 v[2:5], v52, s[14:15]
	global_load_dwordx4 v[6:9], v[14:15], off
	global_load_dwordx4 v[10:13], v16, s[14:15]
	s_nop 0
	global_load_dwordx4 v[14:17], v[22:23], off
	global_load_dwordx4 v[18:21], v24, s[14:15]
	s_nop 0
	global_load_dwordx4 v[22:25], v[32:33], off
	global_load_dwordx4 v[26:29], v34, s[14:15]
	v_lshlrev_b32_e32 v57, 4, v30
	global_load_dwordx4 v[30:33], v[38:39], off
	global_load_dwordx4 v[34:37], v57, s[14:15]
	v_or_b32_e32 v38, 0x1200, v0
	v_add_co_u32_e32 v62, vcc, s2, v46
	v_lshlrev_b32_e32 v58, 4, v38
	v_or_b32_e32 v38, 0x1400, v0
	v_addc_co_u32_e32 v63, vcc, 0, v47, vcc
	s_movk_i32 s2, 0x4000
	v_min_u32_e32 v38, 0x14ff, v38
	v_add_co_u32_e32 v64, vcc, s2, v46
	v_lshlrev_b32_e32 v59, 4, v38
	global_load_dwordx4 v[38:41], v58, s[14:15]
	global_load_dwordx4 v[42:45], v59, s[14:15]
	global_load_dwordx4 v[82:85], v[46:47], off
	global_load_dwordx4 v[86:89], v[46:47], off offset:1024
	global_load_dwordx4 v[90:93], v[46:47], off offset:2048
	global_load_dwordx4 v[94:97], v[46:47], off offset:3072
	global_load_dwordx4 v[98:101], v[48:49], off offset:1024
	global_load_dwordx4 v[102:105], v[48:49], off offset:2048
	global_load_dwordx4 v[106:109], v[60:61], off offset:-4096
	global_load_dwordx4 v[110:113], v[60:61], off
	global_load_dwordx4 v[114:117], v[60:61], off offset:1024
	global_load_dwordx4 v[118:121], v[60:61], off offset:2048
	v_addc_co_u32_e32 v65, vcc, 0, v47, vcc
	global_load_dwordx4 v[122:125], v[60:61], off offset:3072
	global_load_dwordx4 v[126:129], v[64:65], off offset:-4096
	global_load_dwordx4 v[130:133], v[48:49], off offset:3072
	global_load_dwordx4 v[134:137], v[62:63], off offset:1024
	global_load_dwordx4 v[138:141], v[62:63], off offset:2048
	global_load_dwordx4 v[142:145], v[62:63], off offset:3072
	global_load_dwordx4 v[146:149], v[64:65], off
	global_load_dwordx4 v[150:153], v[64:65], off offset:1024
	global_load_dwordx4 v[154:157], v[64:65], off offset:2048
	global_load_dwordx4 v[158:161], v[64:65], off offset:3072
	v_add_co_u32_e32 v46, vcc, 0x5000, v46
	s_movk_i32 s2, 0xff
	s_nop 0
	v_addc_co_u32_e32 v47, vcc, 0, v47, vcc
	global_load_dwordx4 v[162:165], v[46:47], off

.LBB3_63:
	s_cmp_eq_u32 s79, 0
	s_cbranch_scc1 .LBB3_66
	v_add_u32_e32 v231, s21, v211
	ds_read_b128 v[166:169], v231
	s_cmp_lt_u32 s14, s93
	s_cbranch_scc1 .Lgru_l1_mid
	v_exp_f32_e32 v0, v2
	v_exp_f32_e32 v2, v3
	v_exp_f32_e32 v3, v4
	v_exp_f32_e32 v4, v5
	v_exp_f32_e32 v5, v6
	v_exp_f32_e32 v6, v7
	v_exp_f32_e32 v7, v8
	v_exp_f32_e32 v8, v9
	v_exp_f32_e32 v9, v10
	v_exp_f32_e32 v10, v11
	v_exp_f32_e32 v11, v12
	v_exp_f32_e32 v12, v13
	v_exp_f32_e32 v13, v14
	v_add_f32_e32 v0, 1.0, v0
	v_exp_f32_e32 v14, v18
	v_exp_f32_e32 v18, v19
	v_exp_f32_e32 v19, v20
	v_exp_f32_e32 v20, v21
	v_exp_f32_e32 v21, v22
	v_exp_f32_e32 v22, v23
	v_exp_f32_e32 v23, v24
	v_exp_f32_e32 v24, v25
	v_exp_f32_e32 v25, v26
	v_exp_f32_e32 v26, v27
	v_exp_f32_e32 v27, v28
	v_exp_f32_e32 v28, v29
	v_exp_f32_e32 v29, v30
	v_add_f32_e32 v30, 1.0, v2
	v_add_f32_e32 v65, 1.0, v11
	v_rcp_f32_e32 v2, v0
	v_add_f32_e32 v79, 1.0, v12
	v_rcp_f32_e32 v12, v65
	v_add_f32_e32 v31, 1.0, v3
	v_rcp_f32_e32 v3, v30
	v_add_f32_e32 v47, 1.0, v6
	v_add_f32_e32 v80, 1.0, v13
	v_rcp_f32_e32 v13, v79
	v_add_f32_e32 v32, 1.0, v4
	v_add_f32_e32 v48, 1.0, v7
	v_rcp_f32_e32 v4, v31
	v_rcp_f32_e32 v7, v47
	v_fma_f32 v0, v2, v34, v66
	v_add_f32_e32 v81, 1.0, v14
	v_rcp_f32_e32 v14, v80
	v_fma_f32 v66, v12, v44, v76
	v_exp_f32_e32 v0, v0
	v_add_f32_e32 v33, 1.0, v5
	v_add_f32_e32 v49, 1.0, v8
	v_rcp_f32_e32 v5, v32
	v_rcp_f32_e32 v8, v48
	v_fma_f32 v31, v3, v35, v67
	v_exp_f32_e32 v66, v66
	v_fma_f32 v67, v13, v45, v77
	v_exp_f32_e32 v31, v31
	v_rcp_f32_e32 v6, v33
	v_fma_f32 v32, v4, v36, v68
	v_fma_f32 v48, v7, v39, v71
	v_exp_f32_e32 v67, v67
	v_fma_f32 v68, v14, v46, v78
	v_exp_f32_e32 v32, v32
	v_exp_f32_e32 v48, v48
	v_add_f32_e32 v0, 1.0, v0
	v_add_f32_e32 v63, 1.0, v9
	v_rcp_f32_e32 v9, v49
	v_fma_f32 v33, v5, v37, v69
	v_fma_f32 v49, v8, v40, v72
	v_exp_f32_e32 v68, v68
	v_add_f32_e32 v76, 1.0, v66
	v_rcp_f32_e32 v66, v0
	v_exp_f32_e32 v33, v33
	v_exp_f32_e32 v49, v49
	v_add_f32_e32 v31, 1.0, v31
	v_fma_f32 v47, v6, v38, v70
	v_add_f32_e32 v77, 1.0, v67
	v_rcp_f32_e32 v67, v31
	v_add_f32_e32 v219, 1.0, v18
	v_rcp_f32_e32 v18, v81
	v_exp_f32_e32 v47, v47
	v_add_f32_e32 v32, 1.0, v32
	v_add_f32_e32 v48, 1.0, v48
	v_add_f32_e32 v78, 1.0, v68
	v_rcp_f32_e32 v68, v32
	v_rcp_f32_e32 v71, v48
	v_fma_f32 v66, v66, -2.0, 1.0
	v_add_f32_e32 v220, 1.0, v19
	v_rcp_f32_e32 v19, v219
	v_add_f32_e32 v33, 1.0, v33
	v_add_f32_e32 v49, 1.0, v49
	v_add_f32_e32 v64, 1.0, v10
	v_sub_f32_e32 v0, v50, v66
	v_rcp_f32_e32 v10, v63
	v_rcp_f32_e32 v69, v33
	v_rcp_f32_e32 v72, v49
	v_fma_f32 v67, v67, -2.0, 1.0
	v_add_f32_e32 v221, 1.0, v20
	v_rcp_f32_e32 v20, v220
	v_add_f32_e32 v47, 1.0, v47
	v_fma_f32 v50, v18, v0, v66
	v_rcp_f32_e32 v11, v64
	v_sub_f32_e32 v0, v51, v67
	v_fma_f32 v63, v9, v41, v73
	v_rcp_f32_e32 v70, v47
	v_fma_f32 v68, v68, -2.0, 1.0
	v_add_f32_e32 v222, 1.0, v21
	v_rcp_f32_e32 v21, v221
	v_exp_f32_e32 v63, v63
	v_fma_f32 v51, v19, v0, v67
	v_fma_f32 v64, v10, v42, v74
	v_sub_f32_e32 v0, v52, v68
	v_fma_f32 v69, v69, -2.0, 1.0
	v_add_f32_e32 v223, 1.0, v22
	v_rcp_f32_e32 v22, v222
	v_exp_f32_e32 v64, v64
	v_fma_f32 v52, v20, v0, v68
	v_fma_f32 v65, v11, v43, v75
	v_sub_f32_e32 v0, v53, v69
	v_fma_f32 v70, v70, -2.0, 1.0
	v_add_f32_e32 v224, 1.0, v23
	v_rcp_f32_e32 v23, v223
	v_exp_f32_e32 v65, v65
	v_add_f32_e32 v63, 1.0, v63
	v_fma_f32 v53, v21, v0, v69
	v_rcp_f32_e32 v73, v63
	v_sub_f32_e32 v0, v54, v70
	v_fma_f32 v71, v71, -2.0, 1.0
	v_add_f32_e32 v225, 1.0, v24
	v_rcp_f32_e32 v24, v224
	v_add_f32_e32 v64, 1.0, v64
	v_fma_f32 v54, v22, v0, v70
	v_rcp_f32_e32 v74, v64
	v_sub_f32_e32 v0, v55, v71
	v_fma_f32 v72, v72, -2.0, 1.0
	v_add_f32_e32 v226, 1.0, v25
	v_rcp_f32_e32 v25, v225
	v_add_f32_e32 v65, 1.0, v65
	v_fma_f32 v55, v23, v0, v71
	v_rcp_f32_e32 v75, v65
	v_sub_f32_e32 v0, v56, v72
	v_fma_f32 v73, v73, -2.0, 1.0
	v_add_f32_e32 v227, 1.0, v26
	v_rcp_f32_e32 v26, v226
	v_fma_f32 v56, v24, v0, v72
	v_rcp_f32_e32 v76, v76
	v_sub_f32_e32 v0, v57, v73
	v_fma_f32 v74, v74, -2.0, 1.0
	v_add_f32_e32 v228, 1.0, v27
	v_rcp_f32_e32 v27, v227
	v_fma_f32 v57, v25, v0, v73
	v_rcp_f32_e32 v77, v77
	v_sub_f32_e32 v0, v58, v74
	v_fma_f32 v75, v75, -2.0, 1.0
	v_add_f32_e32 v229, 1.0, v28
	v_rcp_f32_e32 v28, v228
	v_fma_f32 v58, v26, v0, v74
	v_rcp_f32_e32 v78, v78
	v_sub_f32_e32 v0, v59, v75
	v_fma_f32 v76, v76, -2.0, 1.0
	v_add_f32_e32 v230, 1.0, v29
	v_rcp_f32_e32 v29, v229
	v_fma_f32 v59, v27, v0, v75
	v_rcp_f32_e32 v30, v230
	v_sub_f32_e32 v0, v60, v76
	v_fma_f32 v77, v77, -2.0, 1.0
	v_fma_f32 v60, v28, v0, v76
	v_fma_f32 v78, v78, -2.0, 1.0
	v_sub_f32_e32 v0, v61, v77
	s_nop 0
	v_fma_f32 v61, v29, v0, v77
	v_sub_f32_e32 v0, v62, v78
	s_nop 0
	v_fma_f32 v62, v30, v0, v78
	v_cvt_pk_f16_f32 v33, v52, v53
	v_cvt_f16_f32_e32 v0, v62
	v_cvt_pk_f16_f32 v32, v50, v51
	v_cvt_pk_f16_f32 v49, v56, v57
	v_cvt_pk_f16_f32 v48, v54, v55
	ds_write2_b64 v210, v[32:33], v[48:49] offset1:2
	v_cvt_pk_f16_f32 v33, v60, v61
	v_cvt_pk_f16_f32 v32, v58, v59
	v_perm_b32 v0, v208, v0, s15
	ds_write_b64 v210, v[32:33] offset:32
	ds_write_b64 v218, v[0:1]

.Lgru_predump:
	s_cmp_lg_u32 s92, 0
	s_cbranch_scc1 .Lgru_dump
	s_mov_b32 s92, 1
	s_movk_i32 s14, 27
	s_movk_i32 s50, 28
	s_branch .LBB3_63
.Lgru_dump:
	s_lshl_b32 s58, s54, 17
	s_add_u32 s58, s58, 0x1120000
	s_add_u32 s58, s16, s58
	s_addc_u32 s59, s17, 0
	v_lshlrev_b32_e32 v219, 4, v248
	v_readfirstlane_b32 s55, v248
	global_store_dwordx4 v219, v[50:53], s[58:59] sc0 sc1
	v_add_u32_e32 v221, 0x2000, v219
	global_store_dwordx4 v221, v[54:57], s[58:59] sc0 sc1
	v_add_u32_e32 v220, 0x4000, v219
	global_store_dwordx4 v220, v[58:61], s[58:59] sc0 sc1
	v_add_u32_e32 v221, 0x6000, v219
	global_store_dwordx4 v221, v[62:65], s[58:59] sc0 sc1
.Lgru_dump_r3:
	v_add_u32_e32 v220, 0x400, v248
	v_min_u32_e32 v220, 0x59f, v220
	v_lshlrev_b32_e32 v220, 4, v220
	v_add_u32_e32 v221, 0x1fc00, v219
	v_add_u32_e32 v222, 0x1fc00, v220
	ds_read_b128 v[224:227], v221
	ds_read_b128 v[228:231], v221 offset:8192
	ds_read_b128 v[232:235], v222
	v_add_u32_e32 v221, 0x18000, v219
	v_add_u32_e32 v222, 0x1a000, v219
	v_add_u32_e32 v223, 0x18000, v220
	s_waitcnt lgkmcnt(2)
	global_store_dwordx4 v221, v[224:227], s[58:59] sc0 sc1
	s_waitcnt lgkmcnt(1)
	global_store_dwordx4 v222, v[228:231], s[58:59] sc0 sc1
	s_waitcnt lgkmcnt(0)
	global_store_dwordx4 v223, v[232:235], s[58:59] sc0 sc1
	s_add_i32 s61, s54, 1
	s_branch .Lgru_tile_end

.Lgru_rs_wait:
	s_barrier
	v_mov_b32_e32 v220, 0x27300
	ds_read_b32 v220, v220
	s_waitcnt lgkmcnt(0)
	v_readfirstlane_b32 s57, v220
	s_nop 3
	s_cmp_eq_u32 s57, 0
	s_cbranch_scc1 .Lgru_rs_fallback
	global_load_dwordx4 v[50:53], v219, s[58:59] sc0 sc1
	v_add_u32_e32 v221, 0x2000, v219
	global_load_dwordx4 v[54:57], v221, s[58:59] sc0 sc1
	v_add_u32_e32 v220, 0x4000, v219
	global_load_dwordx4 v[58:61], v220, s[58:59] sc0 sc1
	v_add_u32_e32 v221, 0x6000, v219
	global_load_dwordx4 v[62:65], v221, s[58:59] sc0 sc1
.Lgru_rs_r3:
	v_add_u32_e32 v220, 0x400, v248
	v_min_u32_e32 v220, 0x59f, v220
	v_lshlrev_b32_e32 v220, 4, v220
	v_add_u32_e32 v221, 0x18000, v219
	v_add_u32_e32 v222, 0x1a000, v219
	v_add_u32_e32 v223, 0x18000, v220
	global_load_dwordx4 v[224:227], v221, s[58:59] sc0 sc1
	global_load_dwordx4 v[228:231], v222, s[58:59] sc0 sc1
	global_load_dwordx4 v[232:235], v223, s[58:59] sc0 sc1
	v_add_u32_e32 v221, 0x1fc00, v219
	v_add_u32_e32 v222, 0x1fc00, v220
	s_waitcnt vmcnt(2)
	ds_write_b128 v221, v[224:227]
	s_waitcnt vmcnt(1)
	ds_write_b128 v221, v[228:231] offset:8192
	s_waitcnt vmcnt(0)
	ds_write_b128 v222, v[232:235]
	s_movk_i32 s14, 16
	s_mov_b32 s21, 0
	s_cmp_lt_u32 s72, 0x100
	s_cbranch_scc1 .Lapf_skip_b
	ds_read_b128 v[232:235], v215
	ds_read_b128 v[236:239], v215 offset:7168
	ds_read_b128 v[240:243], v215 offset:14336
	ds_read_b128 v[244:247], v215 offset:1024
	ds_read_b128 v[200:203], v215 offset:8192
